# v62 + dropped the s_waitcnt vmcnt(0) (store acknowledgements) between an attention unit and the weight-copy chunk that follows it
# speedup vs baseline: 1.0014x; 1.0014x over previous
.LBB6_1307:
	v_readlane_b32 s6, v254, 13
	v_readlane_b32 s7, v254, 14
	v_mov_b32_e32 v167, v0
	s_waitcnt lgkmcnt(0)
	s_barrier
	v_readfirstlane_b32 s98, v0
	s_nop 0
	s_bitcmp1_b32 s98, 8
	s_cbranch_scc0 .Ldephase_b
	s_sleep 80
